# copy shares shifted away from classes 1/2: trims L0 21,21,9 L1 34,34,17
# speedup vs baseline: 1.0044x; 1.0044x over previous
.LBB0_1363:
.LBB0_1365:
.LBB0_1366:
.LBB0_1368:
.LBB0_1370:
.LBB0_1372:
.LBB0_1374:
.LBB0_1378:
.LBB0_1380:
.LBB0_1381:
.LBB0_1383:
.LBB0_1385:
.LBB0_1387:
.LBB0_1388:
.LBB0_1390:
.LBB0_1392:
.LBB0_1393:
.LBB0_1394:
.LBB0_1395:
.LBB0_1397:
.LBB0_1401:
.LBB0_1403:
.LBB0_1404:
.LBB0_1406:
.LBB0_1408:
.LBB0_1410:
.LBB0_1411:
.LBB0_1414:
.LBB0_1418:
.LBB0_1420:
.LBB0_1421:
.LBB0_1423:
.LBB0_1425:
.Lmoe_site_A:
	s_nop 1
	v_writelane_b32 v255, s0, 0
	v_writelane_b32 v255, s1, 1
	v_writelane_b32 v255, s2, 2
	v_writelane_b32 v255, s3, 3
	v_writelane_b32 v255, s4, 4
	v_writelane_b32 v255, s5, 5
	v_writelane_b32 v255, s6, 6
	v_writelane_b32 v255, s7, 7
	v_writelane_b32 v255, s8, 8
	v_writelane_b32 v255, s9, 9
	v_writelane_b32 v255, s10, 10
	v_writelane_b32 v255, s11, 11
	v_writelane_b32 v255, s12, 12
	v_writelane_b32 v255, s13, 13
	v_writelane_b32 v255, s14, 14
	v_writelane_b32 v255, s15, 15
	v_writelane_b32 v255, s16, 16
	v_writelane_b32 v255, s17, 17
	v_writelane_b32 v255, s18, 18
	v_writelane_b32 v255, s19, 19
	v_writelane_b32 v255, s20, 20
	v_writelane_b32 v255, s21, 21
	v_writelane_b32 v255, s22, 22
	v_writelane_b32 v255, s23, 23
	v_writelane_b32 v255, s24, 24
	v_writelane_b32 v255, s25, 25
	v_writelane_b32 v255, s26, 26
	v_writelane_b32 v255, s27, 27
	v_writelane_b32 v255, s28, 28
	v_writelane_b32 v255, s29, 29
	v_writelane_b32 v255, s30, 30
	v_writelane_b32 v255, s31, 31
	v_writelane_b32 v255, s32, 32
	v_writelane_b32 v255, s33, 33
	v_writelane_b32 v255, s34, 34
	v_writelane_b32 v255, s35, 35
	s_movk_i32 s0, 0
	s_movk_i32 s2, 16
	s_mov_b32 s4, 0x7800
	s_mov_b32 s5, 0xd200
	s_mov_b32 s34, 0xb800
	s_branch .Lmoe_p4
.Lmoe_site_B:
	s_nop 1
	v_writelane_b32 v255, s0, 0
	v_writelane_b32 v255, s1, 1
	v_writelane_b32 v255, s2, 2
	v_writelane_b32 v255, s3, 3
	v_writelane_b32 v255, s4, 4
	v_writelane_b32 v255, s5, 5
	v_writelane_b32 v255, s6, 6
	v_writelane_b32 v255, s7, 7
	v_writelane_b32 v255, s8, 8
	v_writelane_b32 v255, s9, 9
	v_writelane_b32 v255, s10, 10
	v_writelane_b32 v255, s11, 11
	v_writelane_b32 v255, s12, 12
	v_writelane_b32 v255, s13, 13
	v_writelane_b32 v255, s14, 14
	v_writelane_b32 v255, s15, 15
	v_writelane_b32 v255, s16, 16
	v_writelane_b32 v255, s17, 17
	v_writelane_b32 v255, s18, 18
	v_writelane_b32 v255, s19, 19
	v_writelane_b32 v255, s20, 20
	v_writelane_b32 v255, s21, 21
	v_writelane_b32 v255, s22, 22
	v_writelane_b32 v255, s23, 23
	v_writelane_b32 v255, s24, 24
	v_writelane_b32 v255, s25, 25
	v_writelane_b32 v255, s26, 26
	v_writelane_b32 v255, s27, 27
	v_writelane_b32 v255, s28, 28
	v_writelane_b32 v255, s29, 29
	v_writelane_b32 v255, s30, 30
	v_writelane_b32 v255, s31, 31
	v_writelane_b32 v255, s32, 32
	v_writelane_b32 v255, s33, 33
	v_writelane_b32 v255, s34, 34
	v_writelane_b32 v255, s35, 35
	s_movk_i32 s0, 1
	s_movk_i32 s2, 8
	s_mov_b32 s4, 0x800
	s_mov_b32 s5, 0x6600
	s_mov_b32 s34, 0x5600
	s_branch .Lmoe_p4

.Lmoe_site_E:
	s_nop 1
	v_writelane_b32 v255, s0, 0
	v_writelane_b32 v255, s1, 1
	v_writelane_b32 v255, s2, 2
	v_writelane_b32 v255, s3, 3
	v_writelane_b32 v255, s4, 4
	v_writelane_b32 v255, s5, 5
	v_writelane_b32 v255, s6, 6
	v_writelane_b32 v255, s7, 7
	v_writelane_b32 v255, s8, 8
	v_writelane_b32 v255, s9, 9
	v_writelane_b32 v255, s10, 10
	v_writelane_b32 v255, s11, 11
	v_writelane_b32 v255, s12, 12
	v_writelane_b32 v255, s13, 13
	v_writelane_b32 v255, s14, 14
	v_writelane_b32 v255, s15, 15
	v_writelane_b32 v255, s16, 16
	v_writelane_b32 v255, s17, 17
	v_writelane_b32 v255, s18, 18
	v_writelane_b32 v255, s19, 19
	v_writelane_b32 v255, s20, 20
	v_writelane_b32 v255, s21, 21
	v_writelane_b32 v255, s22, 22
	v_writelane_b32 v255, s23, 23
	v_writelane_b32 v255, s24, 24
	v_writelane_b32 v255, s25, 25
	v_writelane_b32 v255, s26, 26
	v_writelane_b32 v255, s27, 27
	v_writelane_b32 v255, s28, 28
	v_writelane_b32 v255, s29, 29
	v_writelane_b32 v255, s30, 30
	v_writelane_b32 v255, s31, 31
	v_writelane_b32 v255, s32, 32
	v_writelane_b32 v255, s33, 33
	v_writelane_b32 v255, s34, 34
	v_writelane_b32 v255, s35, 35
	s_movk_i32 s0, 3
	s_movk_i32 s2, 24
	s_mov_b32 s4, 0xfc00
	s_mov_b32 s5, 0x15600
	s_mov_b32 s34, 0x13c00
	s_branch .Lmoe_p4
.Lmoe_site_T1:
	s_nop 1
	v_writelane_b32 v255, s0, 0
	v_writelane_b32 v255, s1, 1
	v_writelane_b32 v255, s2, 2
	v_writelane_b32 v255, s3, 3
	v_writelane_b32 v255, s4, 4
	v_writelane_b32 v255, s5, 5
	v_writelane_b32 v255, s6, 6
	v_writelane_b32 v255, s7, 7
	v_writelane_b32 v255, s8, 8
	v_writelane_b32 v255, s9, 9
	v_writelane_b32 v255, s10, 10
	v_writelane_b32 v255, s11, 11
	v_writelane_b32 v255, s12, 12
	v_writelane_b32 v255, s13, 13
	v_writelane_b32 v255, s14, 14
	v_writelane_b32 v255, s15, 15
	v_writelane_b32 v255, s16, 16
	v_writelane_b32 v255, s17, 17
	v_writelane_b32 v255, s18, 18
	v_writelane_b32 v255, s19, 19
	v_writelane_b32 v255, s20, 20
	v_writelane_b32 v255, s21, 21
	v_writelane_b32 v255, s22, 22
	v_writelane_b32 v255, s23, 23
	v_writelane_b32 v255, s24, 24
	v_writelane_b32 v255, s25, 25
	v_writelane_b32 v255, s26, 26
	v_writelane_b32 v255, s27, 27
	v_writelane_b32 v255, s28, 28
	v_writelane_b32 v255, s29, 29
	v_writelane_b32 v255, s30, 30
	v_writelane_b32 v255, s31, 31
	v_writelane_b32 v255, s32, 32
	v_writelane_b32 v255, s33, 33
	v_writelane_b32 v255, s34, 34
	v_writelane_b32 v255, s35, 35
	s_movk_i32 s0, 4
	v_readlane_b32 s20, v252, 32
	s_nop 3
	s_cmp_eq_u32 s20, 0
	s_cbranch_scc1 .Lmoe_T1_l1
	s_movk_i32 s2, 32
	s_movk_i32 s26, 1792
	s_mov_b32 s27, 0x1200
	s_mov_b32 s28, 0x3c00
	s_mov_b32 s29, 0x6600
	s_mov_b32 s32, 0xc000
	s_mov_b32 s33, 0x11a00
	s_mov_b32 s5, 0x4600
	s_mov_b32 s35, 0x0
	s_movk_i32 s34, 10
	s_branch .Lmoe_tail
.Lmoe_T1_l1:
	s_movk_i32 s2, 32
	s_movk_i32 s26, 1792
	s_mov_b32 s27, 0x2200
	s_mov_b32 s28, 0x6600
	s_mov_b32 s29, 0x1d600
	s_mov_b32 s32, 0x21600
	s_mov_b32 s33, 0x25600
	s_mov_b32 s5, 0xaa00
	s_mov_b32 s35, 0x6400
	s_movk_i32 s34, 10
	s_branch .Lmoe_tail
.Lmoe_site_T2:
	s_nop 1
	v_writelane_b32 v255, s0, 0
	v_writelane_b32 v255, s1, 1
	v_writelane_b32 v255, s2, 2
	v_writelane_b32 v255, s3, 3
	v_writelane_b32 v255, s4, 4
	v_writelane_b32 v255, s5, 5
	v_writelane_b32 v255, s6, 6
	v_writelane_b32 v255, s7, 7
	v_writelane_b32 v255, s8, 8
	v_writelane_b32 v255, s9, 9
	v_writelane_b32 v255, s10, 10
	v_writelane_b32 v255, s11, 11
	v_writelane_b32 v255, s12, 12
	v_writelane_b32 v255, s13, 13
	v_writelane_b32 v255, s14, 14
	v_writelane_b32 v255, s15, 15
	v_writelane_b32 v255, s16, 16
	v_writelane_b32 v255, s17, 17
	v_writelane_b32 v255, s18, 18
	v_writelane_b32 v255, s19, 19
	v_writelane_b32 v255, s20, 20
	v_writelane_b32 v255, s21, 21
	v_writelane_b32 v255, s22, 22
	v_writelane_b32 v255, s23, 23
	v_writelane_b32 v255, s24, 24
	v_writelane_b32 v255, s25, 25
	v_writelane_b32 v255, s26, 26
	v_writelane_b32 v255, s27, 27
	v_writelane_b32 v255, s28, 28
	v_writelane_b32 v255, s29, 29
	v_writelane_b32 v255, s30, 30
	v_writelane_b32 v255, s31, 31
	v_writelane_b32 v255, s32, 32
	v_writelane_b32 v255, s33, 33
	v_writelane_b32 v255, s34, 34
	v_writelane_b32 v255, s35, 35
	s_movk_i32 s0, 5
	v_readlane_b32 s20, v252, 32
	s_nop 3
	s_cmp_eq_u32 s20, 0
	s_cbranch_scc1 .Lmoe_T2_l1
	s_movk_i32 s2, 128
	s_movk_i32 s26, 1024
	s_mov_b32 s27, 0x2200
	s_mov_b32 s28, 0x6600
	s_mov_b32 s29, 0x1d600
	s_mov_b32 s32, 0x21600
	s_mov_b32 s33, 0x25600
	s_mov_b32 s5, 0x4000
	s_mov_b32 s35, 0x0
	s_movk_i32 s34, 16
	s_branch .Lmoe_tail

.Lmoe_site_T3:
	s_nop 1
	v_writelane_b32 v255, s0, 0
	v_writelane_b32 v255, s1, 1
	v_writelane_b32 v255, s2, 2
	v_writelane_b32 v255, s3, 3
	v_writelane_b32 v255, s4, 4
	v_writelane_b32 v255, s5, 5
	v_writelane_b32 v255, s6, 6
	v_writelane_b32 v255, s7, 7
	v_writelane_b32 v255, s8, 8
	v_writelane_b32 v255, s9, 9
	v_writelane_b32 v255, s10, 10
	v_writelane_b32 v255, s11, 11
	v_writelane_b32 v255, s12, 12
	v_writelane_b32 v255, s13, 13
	v_writelane_b32 v255, s14, 14
	v_writelane_b32 v255, s15, 15
	v_writelane_b32 v255, s16, 16
	v_writelane_b32 v255, s17, 17
	v_writelane_b32 v255, s18, 18
	v_writelane_b32 v255, s19, 19
	v_writelane_b32 v255, s20, 20
	v_writelane_b32 v255, s21, 21
	v_writelane_b32 v255, s22, 22
	v_writelane_b32 v255, s23, 23
	v_writelane_b32 v255, s24, 24
	v_writelane_b32 v255, s25, 25
	v_writelane_b32 v255, s26, 26
	v_writelane_b32 v255, s27, 27
	v_writelane_b32 v255, s28, 28
	v_writelane_b32 v255, s29, 29
	v_writelane_b32 v255, s30, 30
	v_writelane_b32 v255, s31, 31
	v_writelane_b32 v255, s32, 32
	v_writelane_b32 v255, s33, 33
	v_writelane_b32 v255, s34, 34
	v_writelane_b32 v255, s35, 35
	s_movk_i32 s0, 6
	v_readlane_b32 s20, v252, 32
	s_nop 3
	s_cmp_eq_u32 s20, 0
	s_cbranch_scc1 .Lmoe_T3_l1
	s_movk_i32 s2, 128
	s_movk_i32 s26, 1024
	s_mov_b32 s27, 0x1200
	s_mov_b32 s28, 0x3c00
	s_mov_b32 s29, 0x6600
	s_mov_b32 s32, 0xc000
	s_mov_b32 s33, 0x11a00
	s_mov_b32 s5, 0x6600
	s_mov_b32 s35, 0x4600
	s_movk_i32 s34, 8
	s_branch .Lmoe_tail
.Lmoe_T3_l1:
	s_movk_i32 s2, 64
	s_movk_i32 s26, 1536
	s_mov_b32 s27, 0x2200
	s_mov_b32 s28, 0x6600
	s_mov_b32 s29, 0x1d600
	s_mov_b32 s32, 0x21600
	s_mov_b32 s33, 0x25600
	s_mov_b32 s5, 0x6400
	s_mov_b32 s35, 0x4000
	s_movk_i32 s34, 6
	s_branch .Lmoe_tail
